# agg fast path: per-node exec mask skips padded (zero-weight) gather slots and their fma groups in 4-slot groups; bit-identical math
# baseline (speedup 1.0000x reference)
.LBB3_109:
	v_mov_b32_e32 v63, v41
	v_or_b32_e32 v1, 8, v60
	v_cmp_gt_i32_e64 s[6:7], v60, v41
	v_cmp_gt_i32_e64 s[8:9], v1, v41
	v_or_b32_e32 v2, 16, v60
	v_or_b32_e32 v3, 24, v60
	v_cndmask_b32_e64 v0, v40, v48, s[6:7]
	v_cndmask_b32_e64 v1, v39, v48, s[8:9]
	v_cmp_gt_i32_e32 vcc, v2, v41
	v_cmp_gt_i32_e64 s[4:5], v3, v41
	v_lshlrev_b32_e32 v0, 7, v0
	v_cndmask_b32_e32 v2, v37, v48, vcc
	v_cndmask_b32_e64 v3, v26, v48, s[4:5]
	v_lshl_add_u32 v37, v60, 3, v49
	v_lshlrev_b32_e32 v1, 7, v1
	ds_write2_b32 v37, v0, v1 offset1:16
	v_lshlrev_b32_e32 v0, 7, v2
	v_lshlrev_b32_e32 v1, 7, v3
	ds_write2_b32 v37, v0, v1 offset0:32 offset1:48
	ds_read2_b32 v[0:1], v49 offset1:2
	ds_read2_b32 v[2:3], v49 offset0:4 offset1:6
	ds_read2_b32 v[4:5], v49 offset0:8 offset1:10
	ds_read2_b32 v[8:9], v49 offset0:12 offset1:14
	s_waitcnt vmcnt(0)
	v_add_f32_e32 v17, v35, v34
	v_mul_f32_e32 v18, 0x3e4ccccd, v17
	v_mov_b32_e32 v16, 0xf149f2ca
	s_waitcnt lgkmcnt(3)
	v_add_u32_e32 v0, v0, v50
	v_add_u32_e32 v1, v1, v50
	global_load_dwordx4 v[28:31], v0, s[16:17]
	global_load_dwordx4 v[24:27], v1, s[16:17]
	s_waitcnt lgkmcnt(2)
	v_add_u32_e32 v0, v2, v50
	v_add_u32_e32 v1, v3, v50
	s_waitcnt lgkmcnt(1)
	v_add_u32_e32 v10, v4, v50
	global_load_dwordx4 v[20:23], v0, s[16:17]
	global_load_dwordx4 v[12:15], v1, s[16:17]
	v_add_u32_e32 v11, v5, v50
	global_load_dwordx4 v[4:7], v10, s[16:17]
	global_load_dwordx4 v[0:3], v11, s[16:17]
	v_add_f32_e32 v10, v35, v36
	v_mul_f32_e32 v11, 0x3e4ccccd, v10
	v_cmp_lt_f32_e64 s[10:11], 0, v10
	v_add_f32_e32 v32, v35, v32
	s_waitcnt lgkmcnt(0)
	v_add_u32_e32 v8, v8, v50
	v_cndmask_b32_e64 v10, v11, v10, s[10:11]
	v_cmp_lt_f32_e64 s[10:11], 0, v17
	v_max_f32_e32 v11, 0xf149f2ca, v10
	v_cndmask_b32_e64 v11, v11, v16, s[6:7]
	v_cndmask_b32_e64 v17, v18, v17, s[10:11]
	v_cndmask_b32_e64 v18, v17, v16, s[8:9]
	v_max_f32_e32 v11, v11, v18
	v_add_f32_e32 v18, v35, v33
	v_mul_f32_e32 v19, 0x3e4ccccd, v18
	v_cmp_lt_f32_e64 s[10:11], 0, v18
	v_mul_f32_e32 v33, 0x3e4ccccd, v32
	v_add_u32_e32 v9, v9, v50
	v_cndmask_b32_e64 v18, v19, v18, s[10:11]
	v_cmp_lt_f32_e64 s[10:11], 0, v32
	v_cndmask_b32_e32 v19, v18, v16, vcc
	v_mov_b32_e32 v53, 0
	v_cndmask_b32_e64 v32, v33, v32, s[10:11]
	v_cndmask_b32_e64 v16, v32, v16, s[4:5]
	v_max3_f32 v11, v11, v19, v16
	v_mov_b32_e32 v58, 0
	v_mov_b32_e32 v59, 0
	v_mov_b32_dpp v16, v11 quad_perm:[1,0,3,2] row_mask:0xf bank_mask:0xf bound_ctrl:1
	v_max_f32_e32 v16, v16, v16
	v_max_f32_e32 v11, v11, v16
	v_mov_b32_e32 v56, 0
	v_mov_b32_e32 v57, 0
	v_mov_b32_dpp v16, v11 quad_perm:[2,3,0,1] row_mask:0xf bank_mask:0xf bound_ctrl:1
	v_max_f32_e32 v16, v16, v16
	v_max_f32_e32 v11, v11, v16
	v_mov_b32_e32 v54, 0
	v_mov_b32_e32 v55, 0
	v_mov_b32_dpp v16, v11 row_half_mirror row_mask:0xf bank_mask:0xf bound_ctrl:1
	v_max_f32_e32 v16, v16, v16
	v_max_f32_e32 v11, v11, v16
	v_sub_f32_e32 v16, v17, v11
	v_mul_f32_e32 v16, 0x3fb8aa3b, v16
	v_exp_f32_e32 v16, v16
	v_sub_f32_e32 v10, v10, v11
	v_mul_f32_e32 v10, 0x3fb8aa3b, v10
	v_exp_f32_e32 v10, v10
	v_cndmask_b32_e64 v34, v16, 0, s[8:9]
	v_sub_f32_e32 v16, v18, v11
	v_mul_f32_e32 v16, 0x3fb8aa3b, v16
	v_sub_f32_e32 v11, v32, v11
	v_exp_f32_e32 v16, v16
	v_mul_f32_e32 v11, 0x3fb8aa3b, v11
	v_exp_f32_e32 v11, v11
	v_cndmask_b32_e64 v33, v10, 0, s[6:7]
	v_add_f32_e32 v10, 0, v33
	v_add_f32_e32 v10, v10, v34
	v_cndmask_b32_e64 v32, v16, 0, vcc
	v_add_f32_e32 v10, v10, v32
	v_cndmask_b32_e64 v35, v11, 0, s[4:5]
	v_add_f32_e32 v10, v10, v35
	v_mov_b32_e32 v52, 0
	s_mov_b32 s18, 8
	v_add_f32_dpp v10, v10, v10 quad_perm:[1,0,3,2] row_mask:0xf bank_mask:0xf bound_ctrl:1
	s_cmp_lt_i32 s29, 13
	s_nop 0
	v_add_f32_dpp v10, v10, v10 quad_perm:[2,3,0,1] row_mask:0xf bank_mask:0xf bound_ctrl:1
	s_nop 1
	v_add_f32_dpp v10, v10, v10 row_half_mirror row_mask:0xf bank_mask:0xf bound_ctrl:1
	v_add_f32_e32 v36, 0x24e69595, v10
	global_load_dwordx4 v[16:19], v8, s[16:17]
	s_nop 0
	global_load_dwordx4 v[8:11], v9, s[16:17]
	v_div_scale_f32 v39, s[4:5], v36, v36, 1.0
	v_rcp_f32_e32 v40, v39
	s_nop 0
	v_fma_f32 v41, -v39, v40, 1.0
	v_fmac_f32_e32 v40, v41, v40
	v_div_scale_f32 v41, vcc, 1.0, v36, 1.0
	v_mul_f32_e32 v42, v41, v40
	v_fma_f32 v43, -v39, v42, v41
	v_fmac_f32_e32 v42, v43, v40
	v_fma_f32 v39, -v39, v42, v41
	v_div_fmas_f32 v39, v39, v40, v42
	v_div_fixup_f32 v36, v39, v36, 1.0
	v_mul_f32_e32 v33, v36, v33
	v_mul_f32_e32 v34, v36, v34
	ds_write2_b32 v37, v33, v34 offset0:1 offset1:17
	v_mul_f32_e32 v32, v36, v32
	v_mul_f32_e32 v33, v36, v35
	ds_write2_b32 v37, v32, v33 offset0:33 offset1:49
	ds_read2_b32 v[40:41], v49 offset0:1 offset1:3
	ds_read2_b32 v[36:37], v49 offset0:5 offset1:7
	ds_read2_b32 v[34:35], v49 offset0:9 offset1:11
	ds_read2_b32 v[32:33], v49 offset0:13 offset1:15
	s_waitcnt vmcnt(7) lgkmcnt(3)
	v_fma_mix_f32 v58, v28, v40, v58 op_sel:[0,0,0] op_sel_hi:[1,0,0]
	v_fma_mix_f32 v59, v28, v40, v59 op_sel:[1,0,0] op_sel_hi:[1,0,0]
	v_fma_mix_f32 v56, v29, v40, v56 op_sel:[0,0,0] op_sel_hi:[1,0,0]
	v_fma_mix_f32 v57, v29, v40, v57 op_sel:[1,0,0] op_sel_hi:[1,0,0]
	v_fma_mix_f32 v54, v30, v40, v54 op_sel:[0,0,0] op_sel_hi:[1,0,0]
	v_fma_mix_f32 v55, v30, v40, v55 op_sel:[1,0,0] op_sel_hi:[1,0,0]
	v_fma_mix_f32 v52, v31, v40, v52 op_sel:[0,0,0] op_sel_hi:[1,0,0]
	v_fma_mix_f32 v53, v31, v40, v53 op_sel:[1,0,0] op_sel_hi:[1,0,0]
	s_waitcnt vmcnt(6)
	v_fma_mix_f32 v58, v24, v41, v58 op_sel:[0,0,0] op_sel_hi:[1,0,0]
	v_fma_mix_f32 v59, v24, v41, v59 op_sel:[1,0,0] op_sel_hi:[1,0,0]
	v_fma_mix_f32 v56, v25, v41, v56 op_sel:[0,0,0] op_sel_hi:[1,0,0]
	v_fma_mix_f32 v57, v25, v41, v57 op_sel:[1,0,0] op_sel_hi:[1,0,0]
	v_fma_mix_f32 v54, v26, v41, v54 op_sel:[0,0,0] op_sel_hi:[1,0,0]
	v_fma_mix_f32 v55, v26, v41, v55 op_sel:[1,0,0] op_sel_hi:[1,0,0]
	v_fma_mix_f32 v52, v27, v41, v52 op_sel:[0,0,0] op_sel_hi:[1,0,0]
	v_fma_mix_f32 v53, v27, v41, v53 op_sel:[1,0,0] op_sel_hi:[1,0,0]
	s_waitcnt vmcnt(5) lgkmcnt(2)
	v_fma_mix_f32 v58, v20, v36, v58 op_sel:[0,0,0] op_sel_hi:[1,0,0]
	v_fma_mix_f32 v59, v20, v36, v59 op_sel:[1,0,0] op_sel_hi:[1,0,0]
	v_fma_mix_f32 v56, v21, v36, v56 op_sel:[0,0,0] op_sel_hi:[1,0,0]
	v_fma_mix_f32 v57, v21, v36, v57 op_sel:[1,0,0] op_sel_hi:[1,0,0]
	v_fma_mix_f32 v54, v22, v36, v54 op_sel:[0,0,0] op_sel_hi:[1,0,0]
	v_fma_mix_f32 v55, v22, v36, v55 op_sel:[1,0,0] op_sel_hi:[1,0,0]
	v_fma_mix_f32 v52, v23, v36, v52 op_sel:[0,0,0] op_sel_hi:[1,0,0]
	v_fma_mix_f32 v53, v23, v36, v53 op_sel:[1,0,0] op_sel_hi:[1,0,0]
	s_waitcnt vmcnt(4)
	v_fma_mix_f32 v58, v12, v37, v58 op_sel:[0,0,0] op_sel_hi:[1,0,0]
	v_fma_mix_f32 v59, v12, v37, v59 op_sel:[1,0,0] op_sel_hi:[1,0,0]
	v_fma_mix_f32 v56, v13, v37, v56 op_sel:[0,0,0] op_sel_hi:[1,0,0]
	v_fma_mix_f32 v57, v13, v37, v57 op_sel:[1,0,0] op_sel_hi:[1,0,0]
	v_fma_mix_f32 v54, v14, v37, v54 op_sel:[0,0,0] op_sel_hi:[1,0,0]
	v_fma_mix_f32 v55, v14, v37, v55 op_sel:[1,0,0] op_sel_hi:[1,0,0]
	v_fma_mix_f32 v52, v15, v37, v52 op_sel:[0,0,0] op_sel_hi:[1,0,0]
	v_fma_mix_f32 v53, v15, v37, v53 op_sel:[1,0,0] op_sel_hi:[1,0,0]
	s_waitcnt vmcnt(3) lgkmcnt(1)
	v_fma_mix_f32 v58, v4, v34, v58 op_sel:[0,0,0] op_sel_hi:[1,0,0]
	v_fma_mix_f32 v59, v4, v34, v59 op_sel:[1,0,0] op_sel_hi:[1,0,0]
	v_fma_mix_f32 v56, v5, v34, v56 op_sel:[0,0,0] op_sel_hi:[1,0,0]
	v_fma_mix_f32 v57, v5, v34, v57 op_sel:[1,0,0] op_sel_hi:[1,0,0]
	v_fma_mix_f32 v54, v6, v34, v54 op_sel:[0,0,0] op_sel_hi:[1,0,0]
	v_fma_mix_f32 v55, v6, v34, v55 op_sel:[1,0,0] op_sel_hi:[1,0,0]
	v_fma_mix_f32 v52, v7, v34, v52 op_sel:[0,0,0] op_sel_hi:[1,0,0]
	v_fma_mix_f32 v53, v7, v34, v53 op_sel:[1,0,0] op_sel_hi:[1,0,0]
	s_waitcnt vmcnt(2)
	v_fma_mix_f32 v58, v0, v35, v58 op_sel:[0,0,0] op_sel_hi:[1,0,0]
	v_fma_mix_f32 v59, v0, v35, v59 op_sel:[1,0,0] op_sel_hi:[1,0,0]
	v_fma_mix_f32 v56, v1, v35, v56 op_sel:[0,0,0] op_sel_hi:[1,0,0]
	v_fma_mix_f32 v57, v1, v35, v57 op_sel:[1,0,0] op_sel_hi:[1,0,0]
	v_fma_mix_f32 v54, v2, v35, v54 op_sel:[0,0,0] op_sel_hi:[1,0,0]
	v_fma_mix_f32 v55, v2, v35, v55 op_sel:[1,0,0] op_sel_hi:[1,0,0]
	v_fma_mix_f32 v52, v3, v35, v52 op_sel:[0,0,0] op_sel_hi:[1,0,0]
	v_fma_mix_f32 v53, v3, v35, v53 op_sel:[1,0,0] op_sel_hi:[1,0,0]
	s_waitcnt vmcnt(1) lgkmcnt(0)
	v_fma_mix_f32 v58, v16, v32, v58 op_sel:[0,0,0] op_sel_hi:[1,0,0]
	v_fma_mix_f32 v59, v16, v32, v59 op_sel:[1,0,0] op_sel_hi:[1,0,0]
	v_fma_mix_f32 v56, v17, v32, v56 op_sel:[0,0,0] op_sel_hi:[1,0,0]
	v_fma_mix_f32 v57, v17, v32, v57 op_sel:[1,0,0] op_sel_hi:[1,0,0]
	v_fma_mix_f32 v54, v18, v32, v54 op_sel:[0,0,0] op_sel_hi:[1,0,0]
	v_fma_mix_f32 v55, v18, v32, v55 op_sel:[1,0,0] op_sel_hi:[1,0,0]
	v_fma_mix_f32 v52, v19, v32, v52 op_sel:[0,0,0] op_sel_hi:[1,0,0]
	v_fma_mix_f32 v53, v19, v32, v53 op_sel:[1,0,0] op_sel_hi:[1,0,0]
	s_waitcnt vmcnt(0)
	v_fma_mix_f32 v58, v8, v33, v58 op_sel:[0,0,0] op_sel_hi:[1,0,0]
	v_fma_mix_f32 v59, v8, v33, v59 op_sel:[1,0,0] op_sel_hi:[1,0,0]
	v_fma_mix_f32 v56, v9, v33, v56 op_sel:[0,0,0] op_sel_hi:[1,0,0]
	v_fma_mix_f32 v57, v9, v33, v57 op_sel:[1,0,0] op_sel_hi:[1,0,0]
	v_fma_mix_f32 v54, v10, v33, v54 op_sel:[0,0,0] op_sel_hi:[1,0,0]
	v_fma_mix_f32 v55, v10, v33, v55 op_sel:[1,0,0] op_sel_hi:[1,0,0]
	v_fma_mix_f32 v52, v11, v33, v52 op_sel:[0,0,0] op_sel_hi:[1,0,0]
	v_fma_mix_f32 v53, v11, v33, v53 op_sel:[1,0,0] op_sel_hi:[1,0,0]
	s_cbranch_scc1 .LBB3_112
	v_mul_u32_u24_e32 v0, 0x108, v38
	v_add3_u32 v51, s30, v0, 64
.LBB3_111:
	s_add_i32 s46, s18, 4
	v_cmp_ge_i32_e64 s[44:45], v63, s18
	v_cmp_ge_i32_e64 s[48:49], v63, s46
	ds_read2_b64 v[16:19], v51 offset1:1
	ds_read2_b64 v[8:11], v51 offset0:2 offset1:3
	ds_read2_b64 v[4:7], v51 offset0:4 offset1:5
	ds_read2_b64 v[0:3], v51 offset0:6 offset1:7
	s_mov_b32 s4, s29
	s_waitcnt lgkmcnt(3)
	v_add_u32_e32 v12, v16, v50
	v_add_u32_e32 v13, v18, v50
	s_waitcnt lgkmcnt(2)
	v_add_u32_e32 v8, v8, v50
	v_add_u32_e32 v10, v10, v50
	s_waitcnt lgkmcnt(1)
	v_add_u32_e32 v4, v4, v50
	v_add_u32_e32 v6, v6, v50
	s_waitcnt lgkmcnt(0)
	v_add_u32_e32 v0, v0, v50
	v_add_u32_e32 v2, v2, v50
	s_mov_b64 exec, s[44:45]
	global_load_dwordx4 v[44:47], v12, s[16:17]
	global_load_dwordx4 v[40:43], v13, s[16:17]
	global_load_dwordx4 v[36:39], v8, s[16:17]
	global_load_dwordx4 v[32:35], v10, s[16:17]
	s_mov_b64 exec, s[48:49]
	global_load_dwordx4 v[28:31], v4, s[16:17]
	global_load_dwordx4 v[24:27], v6, s[16:17]
	global_load_dwordx4 v[20:23], v0, s[16:17]
	global_load_dwordx4 v[12:15], v2, s[16:17]
	s_mov_b64 exec, -1
	s_add_i32 s18, s18, 8
	s_add_i32 s29, s29, -8
	v_add_u32_e32 v51, 64, v51
	s_cmp_gt_u32 s4, 20
	s_mov_b64 exec, s[44:45]
	s_waitcnt vmcnt(7)
	v_fma_mix_f32 v58, v44, v17, v58 op_sel:[0,0,0] op_sel_hi:[1,0,0]
	v_fma_mix_f32 v59, v44, v17, v59 op_sel:[1,0,0] op_sel_hi:[1,0,0]
	v_fma_mix_f32 v56, v45, v17, v56 op_sel:[0,0,0] op_sel_hi:[1,0,0]
	v_fma_mix_f32 v57, v45, v17, v57 op_sel:[1,0,0] op_sel_hi:[1,0,0]
	v_fma_mix_f32 v54, v46, v17, v54 op_sel:[0,0,0] op_sel_hi:[1,0,0]
	v_fma_mix_f32 v55, v46, v17, v55 op_sel:[1,0,0] op_sel_hi:[1,0,0]
	v_fma_mix_f32 v52, v47, v17, v52 op_sel:[0,0,0] op_sel_hi:[1,0,0]
	v_fma_mix_f32 v53, v47, v17, v53 op_sel:[1,0,0] op_sel_hi:[1,0,0]
	s_waitcnt vmcnt(6)
	v_fma_mix_f32 v58, v40, v19, v58 op_sel:[0,0,0] op_sel_hi:[1,0,0]
	v_fma_mix_f32 v59, v40, v19, v59 op_sel:[1,0,0] op_sel_hi:[1,0,0]
	v_fma_mix_f32 v56, v41, v19, v56 op_sel:[0,0,0] op_sel_hi:[1,0,0]
	v_fma_mix_f32 v57, v41, v19, v57 op_sel:[1,0,0] op_sel_hi:[1,0,0]
	v_fma_mix_f32 v54, v42, v19, v54 op_sel:[0,0,0] op_sel_hi:[1,0,0]
	v_fma_mix_f32 v55, v42, v19, v55 op_sel:[1,0,0] op_sel_hi:[1,0,0]
	v_fma_mix_f32 v52, v43, v19, v52 op_sel:[0,0,0] op_sel_hi:[1,0,0]
	v_fma_mix_f32 v53, v43, v19, v53 op_sel:[1,0,0] op_sel_hi:[1,0,0]
	s_waitcnt vmcnt(5)
	v_fma_mix_f32 v58, v36, v9, v58 op_sel:[0,0,0] op_sel_hi:[1,0,0]
	v_fma_mix_f32 v59, v36, v9, v59 op_sel:[1,0,0] op_sel_hi:[1,0,0]
	v_fma_mix_f32 v56, v37, v9, v56 op_sel:[0,0,0] op_sel_hi:[1,0,0]
	v_fma_mix_f32 v57, v37, v9, v57 op_sel:[1,0,0] op_sel_hi:[1,0,0]
	v_fma_mix_f32 v54, v38, v9, v54 op_sel:[0,0,0] op_sel_hi:[1,0,0]
	v_fma_mix_f32 v55, v38, v9, v55 op_sel:[1,0,0] op_sel_hi:[1,0,0]
	v_fma_mix_f32 v52, v39, v9, v52 op_sel:[0,0,0] op_sel_hi:[1,0,0]
	v_fma_mix_f32 v53, v39, v9, v53 op_sel:[1,0,0] op_sel_hi:[1,0,0]
	s_waitcnt vmcnt(4)
	v_fma_mix_f32 v58, v32, v11, v58 op_sel:[0,0,0] op_sel_hi:[1,0,0]
	v_fma_mix_f32 v59, v32, v11, v59 op_sel:[1,0,0] op_sel_hi:[1,0,0]
	v_fma_mix_f32 v56, v33, v11, v56 op_sel:[0,0,0] op_sel_hi:[1,0,0]
	v_fma_mix_f32 v57, v33, v11, v57 op_sel:[1,0,0] op_sel_hi:[1,0,0]
	v_fma_mix_f32 v54, v34, v11, v54 op_sel:[0,0,0] op_sel_hi:[1,0,0]
	v_fma_mix_f32 v55, v34, v11, v55 op_sel:[1,0,0] op_sel_hi:[1,0,0]
	v_fma_mix_f32 v52, v35, v11, v52 op_sel:[0,0,0] op_sel_hi:[1,0,0]
	v_fma_mix_f32 v53, v35, v11, v53 op_sel:[1,0,0] op_sel_hi:[1,0,0]
	s_mov_b64 exec, s[48:49]
	s_waitcnt vmcnt(3)
	v_fma_mix_f32 v58, v28, v5, v58 op_sel:[0,0,0] op_sel_hi:[1,0,0]
	v_fma_mix_f32 v59, v28, v5, v59 op_sel:[1,0,0] op_sel_hi:[1,0,0]
	v_fma_mix_f32 v56, v29, v5, v56 op_sel:[0,0,0] op_sel_hi:[1,0,0]
	v_fma_mix_f32 v57, v29, v5, v57 op_sel:[1,0,0] op_sel_hi:[1,0,0]
	v_fma_mix_f32 v54, v30, v5, v54 op_sel:[0,0,0] op_sel_hi:[1,0,0]
	v_fma_mix_f32 v55, v30, v5, v55 op_sel:[1,0,0] op_sel_hi:[1,0,0]
	v_fma_mix_f32 v52, v31, v5, v52 op_sel:[0,0,0] op_sel_hi:[1,0,0]
	v_fma_mix_f32 v53, v31, v5, v53 op_sel:[1,0,0] op_sel_hi:[1,0,0]
	s_waitcnt vmcnt(2)
	v_fma_mix_f32 v58, v24, v7, v58 op_sel:[0,0,0] op_sel_hi:[1,0,0]
	v_fma_mix_f32 v59, v24, v7, v59 op_sel:[1,0,0] op_sel_hi:[1,0,0]
	v_fma_mix_f32 v56, v25, v7, v56 op_sel:[0,0,0] op_sel_hi:[1,0,0]
	v_fma_mix_f32 v57, v25, v7, v57 op_sel:[1,0,0] op_sel_hi:[1,0,0]
	v_fma_mix_f32 v54, v26, v7, v54 op_sel:[0,0,0] op_sel_hi:[1,0,0]
	v_fma_mix_f32 v55, v26, v7, v55 op_sel:[1,0,0] op_sel_hi:[1,0,0]
	v_fma_mix_f32 v52, v27, v7, v52 op_sel:[0,0,0] op_sel_hi:[1,0,0]
	v_fma_mix_f32 v53, v27, v7, v53 op_sel:[1,0,0] op_sel_hi:[1,0,0]
	s_waitcnt vmcnt(1)
	v_fma_mix_f32 v58, v20, v1, v58 op_sel:[0,0,0] op_sel_hi:[1,0,0]
	v_fma_mix_f32 v59, v20, v1, v59 op_sel:[1,0,0] op_sel_hi:[1,0,0]
	v_fma_mix_f32 v56, v21, v1, v56 op_sel:[0,0,0] op_sel_hi:[1,0,0]
	v_fma_mix_f32 v57, v21, v1, v57 op_sel:[1,0,0] op_sel_hi:[1,0,0]
	v_fma_mix_f32 v54, v22, v1, v54 op_sel:[0,0,0] op_sel_hi:[1,0,0]
	v_fma_mix_f32 v55, v22, v1, v55 op_sel:[1,0,0] op_sel_hi:[1,0,0]
	v_fma_mix_f32 v52, v23, v1, v52 op_sel:[0,0,0] op_sel_hi:[1,0,0]
	v_fma_mix_f32 v53, v23, v1, v53 op_sel:[1,0,0] op_sel_hi:[1,0,0]
	s_waitcnt vmcnt(0)
	v_fma_mix_f32 v58, v12, v3, v58 op_sel:[0,0,0] op_sel_hi:[1,0,0]
	v_fma_mix_f32 v59, v12, v3, v59 op_sel:[1,0,0] op_sel_hi:[1,0,0]
	v_fma_mix_f32 v56, v13, v3, v56 op_sel:[0,0,0] op_sel_hi:[1,0,0]
	v_fma_mix_f32 v57, v13, v3, v57 op_sel:[1,0,0] op_sel_hi:[1,0,0]
	v_fma_mix_f32 v54, v14, v3, v54 op_sel:[0,0,0] op_sel_hi:[1,0,0]
	v_fma_mix_f32 v55, v14, v3, v55 op_sel:[1,0,0] op_sel_hi:[1,0,0]
	v_fma_mix_f32 v52, v15, v3, v52 op_sel:[0,0,0] op_sel_hi:[1,0,0]
	v_fma_mix_f32 v53, v15, v3, v53 op_sel:[1,0,0] op_sel_hi:[1,0,0]
	s_mov_b64 exec, -1
	s_cbranch_scc1 .LBB3_111
.LBB3_112:
	s_cmp_lt_i32 s29, 9
	s_cbranch_scc1 .LBB3_114
	v_lshl_add_u32 v0, s18, 3, v49
	ds_read2_b64 v[12:15], v0 offset1:1
	ds_read2_b64 v[0:3], v0 offset0:2 offset1:3
	s_waitcnt lgkmcnt(1)
	v_add_u32_e32 v4, v12, v50
	s_waitcnt lgkmcnt(0)
	v_add_u32_e32 v0, v0, v50
	v_cmp_ge_i32_e64 s[44:45], v63, s18
	s_nop 1
	s_mov_b64 exec, s[44:45]
	global_load_dwordx4 v[20:23], v4, s[16:17]
	global_load_dwordx4 v[8:11], v0, s[16:17]
	v_add_u32_e32 v4, v14, v50
	s_waitcnt vmcnt(1)
	v_fma_mix_f32 v58, v20, v13, v58 op_sel:[0,0,0] op_sel_hi:[1,0,0]
	v_fma_mix_f32 v59, v20, v13, v59 op_sel:[1,0,0] op_sel_hi:[1,0,0]
	v_fma_mix_f32 v56, v21, v13, v56 op_sel:[0,0,0] op_sel_hi:[1,0,0]
	v_fma_mix_f32 v57, v21, v13, v57 op_sel:[1,0,0] op_sel_hi:[1,0,0]
	v_fma_mix_f32 v54, v22, v13, v54 op_sel:[0,0,0] op_sel_hi:[1,0,0]
	v_fma_mix_f32 v55, v22, v13, v55 op_sel:[1,0,0] op_sel_hi:[1,0,0]
	v_fma_mix_f32 v52, v23, v13, v52 op_sel:[0,0,0] op_sel_hi:[1,0,0]
	v_fma_mix_f32 v53, v23, v13, v53 op_sel:[1,0,0] op_sel_hi:[1,0,0]
	global_load_dwordx4 v[16:19], v4, s[16:17]
	s_waitcnt vmcnt(0)
	v_fma_mix_f32 v58, v16, v15, v58 op_sel:[0,0,0] op_sel_hi:[1,0,0]
	v_fma_mix_f32 v59, v16, v15, v59 op_sel:[1,0,0] op_sel_hi:[1,0,0]
	v_fma_mix_f32 v56, v17, v15, v56 op_sel:[0,0,0] op_sel_hi:[1,0,0]
	v_fma_mix_f32 v57, v17, v15, v57 op_sel:[1,0,0] op_sel_hi:[1,0,0]
	v_fma_mix_f32 v54, v18, v15, v54 op_sel:[0,0,0] op_sel_hi:[1,0,0]
	v_fma_mix_f32 v55, v18, v15, v55 op_sel:[1,0,0] op_sel_hi:[1,0,0]
	v_fma_mix_f32 v52, v19, v15, v52 op_sel:[0,0,0] op_sel_hi:[1,0,0]
	v_fma_mix_f32 v53, v19, v15, v53 op_sel:[1,0,0] op_sel_hi:[1,0,0]
	v_add_u32_e32 v0, v2, v50
	v_fma_mix_f32 v58, v8, v1, v58 op_sel:[0,0,0] op_sel_hi:[1,0,0]
	v_fma_mix_f32 v59, v8, v1, v59 op_sel:[1,0,0] op_sel_hi:[1,0,0]
	v_fma_mix_f32 v56, v9, v1, v56 op_sel:[0,0,0] op_sel_hi:[1,0,0]
	v_fma_mix_f32 v57, v9, v1, v57 op_sel:[1,0,0] op_sel_hi:[1,0,0]
	v_fma_mix_f32 v54, v10, v1, v54 op_sel:[0,0,0] op_sel_hi:[1,0,0]
	v_fma_mix_f32 v55, v10, v1, v55 op_sel:[1,0,0] op_sel_hi:[1,0,0]
	v_fma_mix_f32 v52, v11, v1, v52 op_sel:[0,0,0] op_sel_hi:[1,0,0]
	v_fma_mix_f32 v53, v11, v1, v53 op_sel:[1,0,0] op_sel_hi:[1,0,0]
	global_load_dwordx4 v[4:7], v0, s[16:17]
	s_waitcnt vmcnt(0)
	v_fma_mix_f32 v58, v4, v3, v58 op_sel:[0,0,0] op_sel_hi:[1,0,0]
	v_fma_mix_f32 v59, v4, v3, v59 op_sel:[1,0,0] op_sel_hi:[1,0,0]
	v_fma_mix_f32 v56, v5, v3, v56 op_sel:[0,0,0] op_sel_hi:[1,0,0]
	v_fma_mix_f32 v57, v5, v3, v57 op_sel:[1,0,0] op_sel_hi:[1,0,0]
	v_fma_mix_f32 v54, v6, v3, v54 op_sel:[0,0,0] op_sel_hi:[1,0,0]
	v_fma_mix_f32 v55, v6, v3, v55 op_sel:[1,0,0] op_sel_hi:[1,0,0]
	v_fma_mix_f32 v52, v7, v3, v52 op_sel:[0,0,0] op_sel_hi:[1,0,0]
	v_fma_mix_f32 v53, v7, v3, v53 op_sel:[1,0,0] op_sel_hi:[1,0,0]
	s_mov_b64 exec, -1

	.amdhsa_kernel _Z10agg_kernelPKDF16_PKfS2_S2_PKiS4_S4_S2_PDF16_S5_S4_i
		.amdhsa_group_segment_fixed_size 8960
		.amdhsa_private_segment_fixed_size 0
		.amdhsa_kernarg_size 92
		.amdhsa_user_sgpr_count 2
		.amdhsa_user_sgpr_dispatch_ptr 0
		.amdhsa_user_sgpr_queue_ptr 0
		.amdhsa_user_sgpr_kernarg_segment_ptr 1
		.amdhsa_user_sgpr_dispatch_id 0
		.amdhsa_user_sgpr_kernarg_preload_length 0
		.amdhsa_user_sgpr_kernarg_preload_offset 0
		.amdhsa_user_sgpr_private_segment_size 0
		.amdhsa_uses_dynamic_stack 0
		.amdhsa_enable_private_segment 0
		.amdhsa_system_sgpr_workgroup_id_x 1
		.amdhsa_system_sgpr_workgroup_id_y 0
		.amdhsa_system_sgpr_workgroup_id_z 0
		.amdhsa_system_sgpr_workgroup_info 0
		.amdhsa_system_vgpr_workitem_id 0
		.amdhsa_next_free_vgpr 64
		.amdhsa_next_free_sgpr 50
		.amdhsa_accum_offset 64
		.amdhsa_reserve_vcc 1
		.amdhsa_float_round_mode_32 0
		.amdhsa_float_round_mode_16_64 0
		.amdhsa_float_denorm_mode_32 3
		.amdhsa_float_denorm_mode_16_64 3
		.amdhsa_dx10_clamp 1
		.amdhsa_ieee_mode 1
		.amdhsa_fp16_overflow 0
		.amdhsa_tg_split 0
		.amdhsa_exception_fp_ieee_invalid_op 0
		.amdhsa_exception_fp_denorm_src 0
		.amdhsa_exception_fp_ieee_div_zero 0
		.amdhsa_exception_fp_ieee_overflow 0
		.amdhsa_exception_fp_ieee_underflow 0
		.amdhsa_exception_fp_ieee_inexact 0
		.amdhsa_exception_int_div_zero 0
	.end_amdhsa_kernel

amdhsa.kernels:
  - .agpr_count:     0
    .args:
      - .offset:         0
        .size:           248
        .value_kind:     by_value
    .group_segment_fixed_size: 0
    .kernarg_segment_align: 8
    .kernarg_segment_size: 248
    .language:       OpenCL C
    .language_version:
      - 2
      - 0
    .max_flat_workgroup_size: 256
    .name:           _Z11prep_kernel8PrepArgs
    .private_segment_fixed_size: 0
    .sgpr_count:     76
    .sgpr_spill_count: 0
    .symbol:         _Z11prep_kernel8PrepArgs.kd
    .uniform_work_group_size: 1
    .uses_dynamic_stack: false
    .vgpr_count:     29
    .vgpr_spill_count: 0
    .wavefront_size: 64
  - .agpr_count:     0
    .args:
      - .actual_access:  read_only
        .address_space:  global
        .offset:         0
        .size:           8
        .value_kind:     global_buffer
      - .actual_access:  read_only
        .address_space:  global
        .offset:         8
        .size:           8
        .value_kind:     global_buffer
      - .actual_access:  read_only
        .address_space:  global
        .offset:         16
        .size:           8
        .value_kind:     global_buffer
      - .actual_access:  write_only
        .address_space:  global
        .offset:         24
        .size:           8
        .value_kind:     global_buffer
      - .actual_access:  write_only
        .address_space:  global
        .offset:         32
        .size:           8
        .value_kind:     global_buffer
      - .actual_access:  write_only
        .address_space:  global
        .offset:         40
        .size:           8
        .value_kind:     global_buffer
      - .address_space:  global
        .offset:         48
        .size:           8
        .value_kind:     global_buffer
    .group_segment_fixed_size: 1952
    .kernarg_segment_align: 8
    .kernarg_segment_size: 56
    .language:       OpenCL C
    .language_version:
      - 2
      - 0
    .max_flat_workgroup_size: 256
    .name:           _Z11slot_kernelPKiS0_S0_PiS1_S1_S1_
    .private_segment_fixed_size: 0
    .sgpr_count:     106
    .sgpr_spill_count: 2
    .symbol:         _Z11slot_kernelPKiS0_S0_PiS1_S1_S1_.kd
    .uniform_work_group_size: 1
    .uses_dynamic_stack: false
    .vgpr_count:     65
    .vgpr_spill_count: 0
    .wavefront_size: 64
  - .agpr_count:     0
    .args:
      - .actual_access:  read_only
        .address_space:  global
        .offset:         0
        .size:           8
        .value_kind:     global_buffer
      - .actual_access:  read_only
        .address_space:  global
        .offset:         8
        .size:           8
        .value_kind:     global_buffer
      - .actual_access:  read_only
        .address_space:  global
        .offset:         16
        .size:           8
        .value_kind:     global_buffer
      - .actual_access:  read_only
        .address_space:  global
        .offset:         24
        .size:           8
        .value_kind:     global_buffer
      - .actual_access:  write_only
        .address_space:  global
        .offset:         32
        .size:           8
        .value_kind:     global_buffer
      - .actual_access:  write_only
        .address_space:  global
        .offset:         40
        .size:           8
        .value_kind:     global_buffer
    .group_segment_fixed_size: 0
    .kernarg_segment_align: 8
    .kernarg_segment_size: 48
    .language:       OpenCL C
    .language_version:
      - 2
      - 0
    .max_flat_workgroup_size: 256
    .name:           _Z13elogit_kernelPKiS0_PKfS2_PfS3_
    .private_segment_fixed_size: 0
    .sgpr_count:     18
    .sgpr_spill_count: 0
    .symbol:         _Z13elogit_kernelPKiS0_PKfS2_PfS3_.kd
    .uniform_work_group_size: 1
    .uses_dynamic_stack: false
    .vgpr_count:     28
    .vgpr_spill_count: 0
    .wavefront_size: 64
  - .agpr_count:     0
    .args:
      - .actual_access:  read_only
        .address_space:  global
        .offset:         0
        .size:           8
        .value_kind:     global_buffer
      - .actual_access:  read_only
        .address_space:  global
        .offset:         8
        .size:           8
        .value_kind:     global_buffer
      - .actual_access:  read_only
        .address_space:  global
        .offset:         16
        .size:           8
        .value_kind:     global_buffer
      - .actual_access:  read_only
        .address_space:  global
        .offset:         24
        .size:           8
        .value_kind:     global_buffer
      - .actual_access:  read_only
        .address_space:  global
        .offset:         32
        .size:           8
        .value_kind:     global_buffer
      - .actual_access:  read_only
        .address_space:  global
        .offset:         40
        .size:           8
        .value_kind:     global_buffer
      - .actual_access:  read_only
        .address_space:  global
        .offset:         48
        .size:           8
        .value_kind:     global_buffer
      - .actual_access:  read_only
        .address_space:  global
        .offset:         56
        .size:           8
        .value_kind:     global_buffer
      - .actual_access:  write_only
        .address_space:  global
        .offset:         64
        .size:           8
        .value_kind:     global_buffer
      - .actual_access:  write_only
        .address_space:  global
        .offset:         72
        .size:           8
        .value_kind:     global_buffer
      - .actual_access:  read_only
        .address_space:  global
        .offset:         80
        .size:           8
        .value_kind:     global_buffer
      - .offset:         88
        .size:           4
        .value_kind:     by_value
    .group_segment_fixed_size: 8960
    .kernarg_segment_align: 8
    .kernarg_segment_size: 92
    .language:       OpenCL C
    .language_version:
      - 2
      - 0
    .max_flat_workgroup_size: 256
    .name:           _Z10agg_kernelPKDF16_PKfS2_S2_PKiS4_S4_S2_PDF16_S5_S4_i
    .private_segment_fixed_size: 0
    .sgpr_count:     56
    .sgpr_spill_count: 0
    .symbol:         _Z10agg_kernelPKDF16_PKfS2_S2_PKiS4_S4_S2_PDF16_S5_S4_i.kd
    .uniform_work_group_size: 1
    .uses_dynamic_stack: false
    .vgpr_count:     64
    .vgpr_spill_count: 0
    .wavefront_size: 64
  - .agpr_count:     0
    .args:
      - .actual_access:  read_only
        .address_space:  global
        .offset:         0
        .size:           8
        .value_kind:     global_buffer
      - .actual_access:  read_only
        .address_space:  global
        .offset:         8
        .size:           8
        .value_kind:     global_buffer
      - .actual_access:  read_only
        .address_space:  global
        .offset:         16
        .size:           8
        .value_kind:     global_buffer
      - .actual_access:  write_only
        .address_space:  global
        .offset:         24
        .size:           8
        .value_kind:     global_buffer
    .group_segment_fixed_size: 2048
    .kernarg_segment_align: 8
    .kernarg_segment_size: 32
    .language:       OpenCL C
    .language_version:
      - 2
      - 0
    .max_flat_workgroup_size: 512
    .name:           _Z11pool_kernelPKDF16_PKiPKfPf
    .private_segment_fixed_size: 0
    .sgpr_count:     34
    .sgpr_spill_count: 0
    .symbol:         _Z11pool_kernelPKDF16_PKiPKfPf.kd
    .uniform_work_group_size: 1
    .uses_dynamic_stack: false
    .vgpr_count:     37
    .vgpr_spill_count: 0
    .wavefront_size: 64
  - .agpr_count:     0
    .args:
      - .actual_access:  write_only
        .address_space:  global
        .offset:         0
        .size:           8
        .value_kind:     global_buffer
    .group_segment_fixed_size: 0
    .kernarg_segment_align: 8
    .kernarg_segment_size: 8
    .language:       OpenCL C
    .language_version:
      - 2
      - 0
    .max_flat_workgroup_size: 512
    .name:           _Z11zero_kernelPi
    .private_segment_fixed_size: 0
    .sgpr_count:     8
    .sgpr_spill_count: 0
    .symbol:         _Z11zero_kernelPi.kd
    .uniform_work_group_size: 1
    .uses_dynamic_stack: false
    .vgpr_count:     2
    .vgpr_spill_count: 0
    .wavefront_size: 64
  - .agpr_count:     0
    .args:
      - .actual_access:  read_only
        .address_space:  global
        .offset:         0
        .size:           8
        .value_kind:     global_buffer
      - .offset:         8
        .size:           4
        .value_kind:     by_value
      - .offset:         12
        .size:           4
        .value_kind:     by_value
      - .offset:         16
        .size:           4
        .value_kind:     by_value
      - .actual_access:  read_only
        .address_space:  global
        .offset:         24
        .size:           8
        .value_kind:     global_buffer
      - .actual_access:  write_only
        .address_space:  global
        .offset:         32
        .size:           8
        .value_kind:     global_buffer
      - .actual_access:  write_only
        .address_space:  global
        .offset:         40
        .size:           8
        .value_kind:     global_buffer
      - .actual_access:  write_only
        .address_space:  global
        .offset:         48
        .size:           8
        .value_kind:     global_buffer
      - .actual_access:  read_only
        .address_space:  global
        .offset:         56
        .size:           8
        .value_kind:     global_buffer
      - .actual_access:  read_only
        .address_space:  global
        .offset:         64
        .size:           8
        .value_kind:     global_buffer
      - .offset:         72
        .size:           4
        .value_kind:     by_value
      - .offset:         76
        .size:           4
        .value_kind:     by_value
      - .offset:         80
        .size:           248
        .value_kind:     by_value
    .group_segment_fixed_size: 117136
    .kernarg_segment_align: 8
    .kernarg_segment_size: 328
    .language:       OpenCL C
    .language_version:
      - 2
      - 0
    .max_flat_workgroup_size: 512
    .name:           _Z11gemm_kernelILb1EEvPKviiiPKDF16_PDF16_PfS5_PKfS7_ii8PrepArgs
    .private_segment_fixed_size: 0
    .sgpr_count:     37
    .sgpr_spill_count: 0
    .symbol:         _Z11gemm_kernelILb1EEvPKviiiPKDF16_PDF16_PfS5_PKfS7_ii8PrepArgs.kd
    .uniform_work_group_size: 1
    .uses_dynamic_stack: false
    .vgpr_count:     233
    .vgpr_spill_count: 0
    .wavefront_size: 64
  - .agpr_count:     0
    .args:
      - .actual_access:  read_only
        .address_space:  global
        .offset:         0
        .size:           8
        .value_kind:     global_buffer
      - .offset:         8
        .size:           4
        .value_kind:     by_value
      - .offset:         12
        .size:           4
        .value_kind:     by_value
      - .offset:         16
        .size:           4
        .value_kind:     by_value
      - .actual_access:  read_only
        .address_space:  global
        .offset:         24
        .size:           8
        .value_kind:     global_buffer
      - .actual_access:  write_only
        .address_space:  global
        .offset:         32
        .size:           8
        .value_kind:     global_buffer
      - .actual_access:  write_only
        .address_space:  global
        .offset:         40
        .size:           8
        .value_kind:     global_buffer
      - .actual_access:  write_only
        .address_space:  global
        .offset:         48
        .size:           8
        .value_kind:     global_buffer
      - .actual_access:  read_only
        .address_space:  global
        .offset:         56
        .size:           8
        .value_kind:     global_buffer
      - .actual_access:  read_only
        .address_space:  global
        .offset:         64
        .size:           8
        .value_kind:     global_buffer
      - .offset:         72
        .size:           4
        .value_kind:     by_value
      - .offset:         76
        .size:           4
        .value_kind:     by_value
      - .offset:         80
        .size:           248
        .value_kind:     by_value
    .group_segment_fixed_size: 117136
    .kernarg_segment_align: 8
    .kernarg_segment_size: 328
    .language:       OpenCL C
    .language_version:
      - 2
      - 0
    .max_flat_workgroup_size: 512
    .name:           _Z11gemm_kernelILb0EEvPKviiiPKDF16_PDF16_PfS5_PKfS7_ii8PrepArgs
    .private_segment_fixed_size: 0
    .sgpr_count:     40
    .sgpr_spill_count: 0
    .symbol:         _Z11gemm_kernelILb0EEvPKviiiPKDF16_PDF16_PfS5_PKfS7_ii8PrepArgs.kd
    .uniform_work_group_size: 1
    .uses_dynamic_stack: false
    .vgpr_count:     179
    .vgpr_spill_count: 0
    .wavefront_size: 64
